# MIX2: expert-weight conversion staggered over five workgroup groups (slot after the last attention unit used too) instead of four, fewer workgroups streaming at once (on top of v34)
# baseline (speedup 1.0000x reference)
.LBB0_273:
	v_readlane_b32 s19, v252, 0
	s_ashr_i32 s11, s19, 31
	s_lshr_b32 s4, s11, 29
	s_add_i32 s4, s19, s4
	s_load_dwordx2 s[22:23], s[0:1], 0xc8
	s_load_dword s20, s[0:1], 0xd8
	s_ashr_i32 s21, s4, 3
	s_and_b32 s4, s4, -8
	s_sub_i32 s24, s19, s4
	s_and_b32 s15, s33, 0xffffffc0
	s_lshr_b32 s4, s24, 31
	s_cmp_gt_i32 s19, -1
	v_writelane_b32 v252, s4, 12
	s_cselect_b64 s[6:7], -1, 0
	s_waitcnt lgkmcnt(0)
	s_add_u32 s4, s22, 0x4200
	s_addc_u32 s5, s23, 0
	s_lshl_b32 s17, s45, 8
	s_add_u32 s2, s2, s17
	v_writelane_b32 v252, s4, 13
	s_addc_u32 s3, s3, 0
	s_load_dwordx8 s[36:43], s[0:1], 0x48
	v_writelane_b32 v252, s5, 14
	s_add_u32 s4, s2, 0x1400
	s_addc_u32 s5, s3, 0
	v_writelane_b32 v252, s4, 15
	s_add_u32 s2, s2, 0x2400
	s_addc_u32 s3, s3, 0
	v_writelane_b32 v252, s5, 16
	v_writelane_b32 v252, s2, 17
	s_mov_b32 s69, 0
	s_mov_b32 s84, 0x39fda000
	v_writelane_b32 v252, s3, 18
	s_add_u32 s2, s22, 0x7400
	s_addc_u32 s3, s23, 0
	v_writelane_b32 v252, s2, 19
	s_mov_b32 s96, 0x394ca1f9
	s_mov_b32 s92, 0xbe2aaaa3
	v_writelane_b32 v252, s3, 20
	s_add_u32 s2, s22, 0x7500
	s_addc_u32 s3, s23, 0
	v_writelane_b32 v252, s2, 21
	s_and_b32 s9, s19, 7
	s_ashr_i32 s25, s19, 5
	v_writelane_b32 v252, s3, 22
	s_bfe_u32 s2, s19, 0x10003
	v_writelane_b32 v252, s2, 23
	s_lshr_b32 s2, s19, 1
	s_and_b32 s2, s2, 12
	s_lshl_b32 s10, s9, 8
	v_writelane_b32 v252, s2, 24
	s_or_b32 s2, s10, 0x8000
	s_lshl_b32 s4, s25, 6
	s_lshl_b32 s33, s9, 12
	s_ashr_i32 s3, s25, 31
	s_ashr_i32 s5, s4, 31
	s_mul_i32 s94, s2, 0x3600
	s_add_u32 s70, s94, 0xd8000
	s_addc_u32 s71, 0, 0
	s_or_b32 s72, s10, 0x80c0
	s_lshl_b32 s2, s19, 9
	s_add_u32 s12, s22, 0xe0a4200
	v_writelane_b32 v252, s3, 25
	s_addc_u32 s13, s23, 0
	v_writelane_b32 v252, s12, 26
	s_mov_b32 s95, s69
	s_mov_b32 s73, s69
	v_writelane_b32 v252, s13, 27
	s_add_u32 s12, s22, 0x2aba4200
	s_addc_u32 s13, s23, 0
	v_writelane_b32 v252, s12, 28
	s_lshl_b32 s3, s20, 9
	v_mov_b32_e32 v1, 0
	v_writelane_b32 v252, s13, 29
	s_add_u32 s12, s22, 0xcfa4200
	v_writelane_b32 v252, s3, 30
	s_addc_u32 s13, s23, 0
	v_writelane_b32 v252, s12, 31
	v_mov_b32_e32 v234, 0x79797979
	v_mov_b32_e32 v235, 0x7f7f7f7f
	v_writelane_b32 v252, s13, 32
	s_add_u32 s12, s22, 0xd824200
	s_addc_u32 s13, s23, 0
	v_writelane_b32 v252, s12, 33
	s_ashr_i32 s3, s19, 3
	s_mul_i32 s8, s3, 52
	s_lshr_b32 s8, s8, 8
	s_mul_i32 s8, s8, 5
	s_sub_i32 s8, s3, s8
	v_writelane_b32 v252, s13, 34
	v_writelane_b32 v252, s8, 35
	s_lshl_b32 s8, s3, 2
	v_writelane_b32 v252, s8, 36
	s_lshl_b32 s26, s19, 3
	s_lshl_b32 s27, s20, 3
	s_lshl_b32 s8, s20, 4
	s_cmpk_gt_i32 s19, 0x7f
	v_writelane_b32 v252, s8, 37
	s_cselect_b64 s[12:13], -1, 0
	v_writelane_b32 v252, s12, 38
	s_and_b32 s8, s3, 7
	v_mov_b32_e32 v236, 1
	v_writelane_b32 v252, s13, 39
	s_lshl_b32 s12, s8, 8
	s_bitset1_b32 s12, 15
	s_cmp_gt_u32 s19, 63
	s_cselect_b64 s[28:29], -1, 0
	v_writelane_b32 v252, s28, 40
	s_lshl_b32 s13, s9, 6
	s_mulk_i32 s8, 0x2200
	v_writelane_b32 v252, s29, 41
	v_writelane_b32 v252, s13, 42
	s_bfe_u32 s13, s19, 0x10002
	s_or_b32 s8, s8, s13
	s_lshl_b32 s8, s8, 6
	s_add_i32 s8, s8, 0x80000
	s_cmpk_gt_i32 s19, 0x1ff
	s_cselect_b64 s[28:29], -1, 0
	v_writelane_b32 v252, s28, 43
	s_cmpk_gt_u32 s19, 0x23f
	v_mov_b32_e32 v237, 0x358637bd
	v_writelane_b32 v252, s29, 44
	s_cselect_b64 s[28:29], -1, 0
	s_add_i32 s13, s19, 0xfffffe00
	v_writelane_b32 v252, s28, 45
	s_lshr_b32 s13, s13, 3
	s_addk_i32 s13, 0x80
	v_writelane_b32 v252, s29, 46
	v_writelane_b32 v252, s13, 47
	s_bfe_u32 s13, s19, 0x20001
	v_writelane_b32 v252, s13, 48
	s_and_b32 s13, s19, 1
	s_add_i32 s13, s13, 1
	v_writelane_b32 v252, s13, 49
	s_lshl_b32 s13, s24, 6
	s_lshl_b32 s14, s19, 5
	s_cmp_eq_u32 s19, 0
	v_writelane_b32 v252, s14, 50
	s_cselect_b64 s[28:29], -1, 0
	v_writelane_b32 v252, s28, 51
	s_cmp_lt_i32 s19, 32
	s_mov_b32 s85, 0x33a22169
	v_writelane_b32 v252, s29, 52
	s_cselect_b64 s[28:29], -1, 0
	s_lshl_b32 s14, s19, 2
	v_writelane_b32 v252, s28, 53
	s_add_i32 s16, s14, 0
	s_add_i32 s18, s16, 0x21700
	v_writelane_b32 v252, s29, 54
	s_add_i32 s16, s16, 0x21600
	v_writelane_b32 v252, s18, 55
	s_cmpk_lg_i32 s20, 0x100
	v_writelane_b32 v252, s16, 56
	s_cselect_b64 s[28:29], -1, 0
	s_lshr_b32 s16, s3, 29
	s_add_i32 s16, s3, s16
	v_writelane_b32 v252, s28, 57
	s_and_b32 s14, s14, 28
	s_ashr_i32 s18, s16, 3
	v_writelane_b32 v252, s29, 58
	s_add_i32 s14, s14, s18
	v_writelane_b32 v252, s14, 59
	s_and_b32 s14, s16, -8
	s_lshr_b32 s11, s11, 30
	s_sub_i32 s14, s3, s14
	s_add_i32 s11, s19, s11
	s_lshr_b32 s16, s3, 30
	v_writelane_b32 v252, s14, 60
	s_ashr_i32 s14, s11, 2
	s_add_i32 s16, s3, s16
	v_writelane_b32 v252, s14, 61
	s_and_b32 s14, s26, 56
	s_ashr_i32 s18, s16, 2
	s_add_i32 s14, s14, s18
	v_writelane_b32 v252, s14, 62
	s_and_b32 s14, s16, -4
	s_sub_i32 s3, s3, s14
	v_writelane_b32 v252, s3, 63
	s_add_u32 s3, s22, 0x27c000
	v_writelane_b32 v253, s3, 0
	s_addc_u32 s3, s23, 0
	v_writelane_b32 v253, s3, 1
	s_add_u32 s3, s22, 0x1f4000
	v_writelane_b32 v253, s3, 2
	s_addc_u32 s3, s23, 0
	s_add_u32 s28, s22, 0x3a4200
	v_writelane_b32 v253, s3, 3
	s_addc_u32 s29, s23, 0
	v_writelane_b32 v253, s28, 4
	s_mov_b32 s97, 0x37ccf5ce
	s_mov_b32 s93, 0x3d2aaaa5
	v_writelane_b32 v253, s29, 5
	s_add_u32 s28, s22, 0x200a4200
	s_addc_u32 s29, s23, 0
	v_writelane_b32 v253, s28, 6
	s_add_u32 s3, s22, 0x100000
	v_mov_b32_e32 v238, 0x7d7d7d7d
	v_writelane_b32 v253, s29, 7
	v_writelane_b32 v253, s3, 8
	s_addc_u32 s3, s23, 0
	s_add_u32 s28, s22, 0x8ba4200
	v_writelane_b32 v253, s3, 9
	s_addc_u32 s29, s23, 0
	v_writelane_b32 v253, s28, 10
	v_mov_b32_e32 v241, 0x3600
	v_mov_b32_e32 v242, 0xff800000
	v_writelane_b32 v253, s29, 11
	s_add_u32 s28, s22, 0x43b44200
	s_addc_u32 s29, s23, 0
	v_writelane_b32 v253, s28, 12
	s_add_i32 s2, s15, s2
	s_lshl_b32 s18, s20, 5
	v_writelane_b32 v253, s29, 13
	v_writelane_b32 v253, s2, 14
	s_cmp_lt_i32 s24, 0
	s_mul_i32 s2, s24, 0x41
	s_cselect_b32 s2, s2, s13
	s_add_i32 s2, s2, s21
	s_ashr_i32 s3, s2, 31
	s_lshr_b32 s3, s3, 27
	s_add_i32 s3, s2, s3
	s_and_b32 s13, s3, 0xffe0
	s_sub_i32 s2, s2, s13
	s_bfe_i32 s13, s2, 0x80000
	s_bfe_u32 s13, s13, 0x3000c
	s_add_i32 s13, s2, s13
	s_and_b32 s14, s13, 0xf8
	s_sub_i32 s2, s2, s14
	s_ashr_i32 s3, s3, 5
	v_writelane_b32 v253, s24, 15
	s_lshl_b32 s3, s3, 3
	s_sext_i32_i8 s2, s2
	v_writelane_b32 v253, s21, 16
	s_add_i32 s2, s3, s2
	v_writelane_b32 v253, s2, 17
	s_abs_i32 s2, s20
	v_cvt_f32_u32_e32 v0, s2
	v_writelane_b32 v253, s2, 18
	s_sub_i32 s2, 0, s2
	v_mov_b32_e32 v214, 0x3c08839e
	v_rcp_iflag_f32_e32 v0, v0
	v_mov_b32_e32 v215, 0xbab6061a
	v_not_b32_e32 v244, 63
	v_mov_b32_e32 v240, 0x42800000
	v_mul_f32_e32 v0, 0x4f7ffffe, v0
	v_cvt_u32_f32_e32 v0, v0
	v_mov_b32_e32 v243, 0x40e00000
	s_movk_i32 s88, 0x3600
	s_movk_i32 s76, 0xffe0
	v_readfirstlane_b32 s3, v0
	s_mul_i32 s2, s2, s3
	s_mul_hi_u32 s2, s3, s2
	s_add_i32 s2, s3, s2
	v_writelane_b32 v253, s2, 19
	s_bfe_i32 s2, s13, 0x80000
	s_sext_i32_i16 s2, s2
	s_ashr_i32 s2, s2, 3
	v_writelane_b32 v253, s2, 20
	s_and_b32 s2, s11, -4
	s_sub_i32 s2, s19, s2
	v_writelane_b32 v253, s2, 21
	s_not_b32 s2, s15
	v_writelane_b32 v253, s2, 22
	s_ashr_i32 s2, s20, 31
	s_add_u32 s89, s22, 0x4400
	v_writelane_b32 v253, s2, 23
	s_addc_u32 s91, s23, 0
	s_lshl_b32 s2, s44, 8
	s_add_i32 s2, s2, 0
	s_add_i32 s2, s2, 0x15100
	v_writelane_b32 v253, s2, 24
	v_writelane_b32 v253, s25, 25
	s_mul_i32 s3, s25, 0x744
	s_waitcnt lgkmcnt(0)
	s_add_u32 s22, s38, s3
	v_writelane_b32 v253, s36, 26
	s_mul_hi_i32 s2, s25, 0x744
	s_addc_u32 s23, s39, s2
	v_writelane_b32 v253, s37, 27
	v_writelane_b32 v253, s38, 28
	v_writelane_b32 v253, s39, 29
	v_writelane_b32 v253, s40, 30
	v_writelane_b32 v253, s41, 31
	v_writelane_b32 v253, s42, 32
	v_writelane_b32 v253, s43, 33
	v_writelane_b32 v253, s22, 34
	s_mul_i32 s2, s12, 0x3600
	s_or_b32 s10, s10, 0x8040
	v_writelane_b32 v253, s23, 35
	v_writelane_b32 v253, s2, 36
	s_mul_i32 s2, s12, 0xc00
	v_writelane_b32 v253, s2, 37
	s_lshl_b32 s2, s19, 1
	s_and_b32 s11, s2, 48
	v_writelane_b32 v253, s10, 38
	s_mul_i32 s10, s9, 0x2200
	v_writelane_b32 v253, s10, 39
	s_sub_i32 s10, 0, s11
	v_writelane_b32 v253, s10, 40
	s_xor_b32 s10, s11, -7
	v_writelane_b32 v253, s10, 41
	v_writelane_b32 v253, s11, 42
	s_xor_b32 s10, s11, -8
	v_writelane_b32 v253, s10, 43
	s_lshl_b32 s10, s20, 12
	s_mul_i32 s2, s9, 0x3600000
	s_mul_i32 s9, s9, 0x110000
	v_writelane_b32 v253, s10, 44
	s_lshl_b32 s10, s20, 15
	v_writelane_b32 v253, s10, 45
	s_add_u32 s9, s9, 0xd0a0200
	v_writelane_b32 v253, s9, 46
	s_addc_u32 s9, 0, 0
	v_writelane_b32 v253, s9, 47
	s_xor_b64 s[6:7], s[6:7], -1
	v_writelane_b32 v253, s6, 48
	s_lshl_b64 s[86:87], s[4:5], 1
	s_ashr_i32 s4, s26, 31
	v_writelane_b32 v253, s7, 49
	s_lshl_b32 s6, s8, 1
	v_writelane_b32 v253, s6, 50
	v_writelane_b32 v253, s4, 51
	v_writelane_b32 v253, s26, 52
	v_writelane_b32 v253, s27, 53
	s_add_i32 s4, s26, s27
	v_writelane_b32 v253, s4, 54
	s_add_i32 s4, 0, 0x20600
	v_writelane_b32 v253, s4, 55
	s_add_i32 s4, 0, 0x21610
	v_writelane_b32 v253, s4, 56
	s_add_i32 s4, 0, 0x21710
	v_writelane_b32 v253, s4, 57
	s_add_i32 s4, 0, 0x21620
	v_writelane_b32 v253, s4, 58
	s_add_i32 s4, 0, 0x21720
	v_writelane_b32 v253, s4, 59
	s_add_i32 s4, 0, 0x21630
	v_writelane_b32 v253, s4, 60
	s_add_i32 s4, 0, 0x21730
	v_writelane_b32 v253, s4, 61
	s_add_i32 s4, 0, 0x21640
	v_writelane_b32 v253, s4, 62
	s_add_i32 s4, 0, 0x21740
	v_writelane_b32 v253, s4, 63
	s_add_i32 s4, 0, 0x21650
	v_writelane_b32 v254, s4, 0
	s_add_i32 s4, 0, 0x21750
	v_writelane_b32 v254, s4, 1
	s_add_i32 s4, 0, 0x21660
	v_writelane_b32 v254, s4, 2
	s_add_i32 s4, 0, 0x21760
	v_writelane_b32 v254, s4, 3
	s_add_i32 s4, 0, 0x21670
	v_writelane_b32 v254, s4, 4
	s_add_i32 s4, 0, 0x21770
	v_writelane_b32 v254, s4, 5
	s_add_i32 s4, 0, 0x21780
	v_writelane_b32 v254, s4, 6
	s_add_i32 s4, 0, 0x20480
	v_writelane_b32 v254, s4, 7
	s_add_i32 s4, 0, 0x20440
	v_writelane_b32 v254, s4, 8
	s_add_i32 s4, 0, 0x23800
	v_writelane_b32 v254, s4, 9
	s_add_i32 s4, 0, 0x23000
	v_writelane_b32 v254, s4, 10
	s_mov_b32 s5, 1
	s_ashr_i32 s19, s18, 31
	v_writelane_b32 v254, s4, 11
	s_load_dwordx8 s[36:43], s[0:1], 0xa8
	s_mov_b32 s3, s69
	v_writelane_b32 v254, s5, 12
	s_lshl_b64 s[4:5], s[18:19], 11
	v_writelane_b32 v254, s4, 13
	s_add_i32 s77, 0, 0x14900
	s_movk_i32 s78, 0xffd0
	v_writelane_b32 v254, s5, 14
	s_lshl_b64 s[4:5], s[18:19], 12
	v_writelane_b32 v254, s4, 15
	s_movk_i32 s79, 0xffef
	s_movk_i32 s80, 0x7fff
	v_writelane_b32 v254, s5, 16
	s_lshl_b64 s[4:5], s[18:19], 10
	v_writelane_b32 v254, s4, 17
	s_mov_b32 s82, 0x3fffc00
	s_mov_b64 s[66:67], 0x80
	v_writelane_b32 v254, s5, 18
	s_mov_b32 s4, s18
	v_writelane_b32 v254, s4, 19
	s_mov_b32 s14, 0x3e38aa3b
	s_mov_b32 s16, 0x3fb8aa3b
	v_writelane_b32 v254, s5, 20
	s_lshl_b64 s[4:5], s[18:19], 4
	v_writelane_b32 v254, s4, 21
	s_mov_b64 s[18:19], 0x800
	s_mov_b64 s[20:21], 0x1b0000
	v_writelane_b32 v254, s5, 22
	s_load_dwordx4 s[4:7], s[0:1], 0x30
	s_mov_b32 s22, 0x41000000
	s_mov_b64 s[24:25], 0x8000
	s_mov_b32 s8, s69
	s_waitcnt lgkmcnt(0)
	v_writelane_b32 v254, s4, 23
	s_nop 1
	v_writelane_b32 v254, s5, 24
	v_writelane_b32 v254, s6, 25
	v_writelane_b32 v254, s7, 26
	s_load_dwordx4 s[4:7], s[0:1], 0x90
	s_waitcnt lgkmcnt(0)
	v_writelane_b32 v254, s4, 27
	s_nop 1
	v_writelane_b32 v254, s5, 28
	v_writelane_b32 v254, s6, 29
	v_writelane_b32 v254, s7, 30
	v_writelane_b32 v254, s36, 31
	s_nop 1
	v_writelane_b32 v254, s37, 32
	v_writelane_b32 v254, s38, 33
	v_writelane_b32 v254, s39, 34
	v_writelane_b32 v254, s40, 35
	v_writelane_b32 v254, s41, 36
	v_writelane_b32 v254, s42, 37
	v_writelane_b32 v254, s43, 38
	s_branch .LBB0_277
